# n17_early2
# speedup vs baseline: 1.0269x; 1.0083x over previous
.LBB2_15:
	v_ashrrev_i32_e32 v163, 31, v162
	v_lshl_or_b32 v164, s30, 4, v132
	v_lshlrev_b64 v[130:131], 11, v[162:163]
	v_mov_b32_e32 v167, 0
	s_waitcnt lgkmcnt(0)
	s_mov_b64 s[50:51], s[0:1]
	v_lshl_add_u64 v[130:131], s[0:1], 0, v[130:131]
	v_lshlrev_b32_e32 v166, 4, v164
	v_lshl_add_u64 v[168:169], v[130:131], 0, v[166:167]
	global_load_dwordx2 v[170:171], v[168:169], off nt
	v_lshlrev_b32_e32 v142, 4, v140
	v_cmp_gt_u32_e64 s[2:3], 16, v140
	v_mov_b32_e32 v140, 0x10000
	v_lshlrev_b32_e32 v130, 8, v139
	v_lshlrev_b32_e32 v131, 4, v132
	v_lshlrev_b32_e32 v132, 3, v138
	v_lshl_or_b32 v177, v138, 14, v142
	v_lshl_or_b32 v139, v139, 11, v140
	v_lshlrev_b32_e32 v140, 10, v138
	v_xor_b32_e32 v138, 1, v138
	v_lshlrev_b32_e32 v141, 12, v1
	v_lshlrev_b32_e32 v138, 10, v138
	v_or3_b32 v179, v139, v138, v142
	v_add_u32_e32 v138, 0x1000, v141
	v_and_b32_e32 v180, 0x3000, v138
	v_add_u32_e32 v138, 0x1400, v141
	v_and_b32_e32 v181, 0x3400, v138
	v_add_u32_e32 v138, 0x1800, v141
	v_and_b32_e32 v182, 0x3800, v138
	v_add_u32_e32 v138, 0x1c00, v141
	v_and_b32_e32 v183, 0x3c00, v138
	s_movk_i32 s4, 0x2000
	v_mov_b32_e32 v138, 0x3000
	v_bitop3_b32 v184, v141, s4, v138 bitop3:0x6c
	v_add_u32_e32 v138, 0x2400, v141
	v_and_b32_e32 v185, 0x3400, v138
	v_add_u32_e32 v138, 0x2800, v141
	v_and_b32_e32 v186, 0x3800, v138
	v_add_u32_e32 v138, 0x2c00, v141
	v_and_b32_e32 v187, 0x3c00, v138
	v_add_u32_e32 v138, 0x3000, v141
	v_and_b32_e32 v188, 0x3000, v138
	v_add_u32_e32 v138, 0x3400, v141
	s_and_b32 s9, s7, 0xffff
	v_cmp_eq_u32_e32 vcc, s14, v133
	v_lshl_or_b32 v131, s16, 10, v131
	s_movk_i32 s0, 0x100
	v_lshlrev_b32_e32 v166, 12, v164
	v_and_b32_e32 v189, 0x3400, v138
	v_add_u32_e32 v138, 0x3800, v141
	s_cmp_lg_u64 vcc, exec
	v_lshl_add_u32 v131, s30, 15, v131
	v_cmp_gt_u32_e64 s[0:1], s0, v0
	v_lshl_add_u64 v[0:1], s[12:13], 0, v[166:167]
	v_and_b32_e32 v190, 0x3800, v138
	v_add_u32_e32 v138, 0x3c00, v141
	v_mov_b32_e32 v172, -1
	s_mov_b32 s11, 0x20000
	s_mov_b32 s10, 0x200400
	s_mov_b32 s8, s6
	s_cselect_b64 s[14:15], -1, 0
	v_or3_b32 v165, v131, v132, v130
	s_mov_b32 s17, 0
	v_cndmask_b32_e64 v133, 0, v137, s[0:1]
	v_cndmask_b32_e64 v132, 0, v136, s[0:1]
	v_cndmask_b32_e64 v131, 0, v135, s[0:1]
	v_cndmask_b32_e64 v130, 0, v134, s[0:1]
	v_cndmask_b32_e64 v137, v137, 0, s[0:1]
	v_cndmask_b32_e64 v136, v136, 0, s[0:1]
	v_cndmask_b32_e64 v135, v135, 0, s[0:1]
	v_cndmask_b32_e64 v134, v134, 0, s[0:1]
	v_or_b32_e32 v176, v141, v142
	v_lshl_add_u64 v[0:1], v[162:163], 2, v[0:1]
	v_or3_b32 v178, v139, v140, v142
	v_and_b32_e32 v191, 0x3c00, v138
	s_mov_b64 s[24:25], 0
	s_mov_b64 s[18:19], 0x400
	s_mov_b64 s[20:21], 0x800
	s_mov_b64 s[22:23], 0xc00
	s_mov_b32 s31, 0x40004000
	v_mov_b32_e32 v173, v172
	v_mov_b32_e32 v192, 0
	v_mov_b32_e32 v193, 0
	s_mov_b32 s33, 0
	v_add_u32_e32 v180, v180, v177
	v_add_u32_e32 v181, v181, v177
	v_add_u32_e32 v182, v182, v177
	v_add_u32_e32 v183, v183, v177
	v_add_u32_e32 v184, v184, v177
	v_add_u32_e32 v185, v185, v177
	v_add_u32_e32 v186, v186, v177
	v_add_u32_e32 v187, v187, v177
	v_add_u32_e32 v188, v188, v177
	v_add_u32_e32 v189, v189, v177
	v_add_u32_e32 v190, v190, v177
	v_add_u32_e32 v191, v191, v177
	v_mov_b32_e32 v166, v176
	v_lshlrev_b32_e32 v242, 12, v164
	v_lshl_add_u32 v242, v162, 2, v242
	v_lshlrev_b32_e32 v243, 11, v162
	v_lshl_add_u32 v243, v164, 4, v243
	v_readfirstlane_b32 s42, v176
	s_or_b32 s42, s42, 0x8000
	s_mov_b32 m0, s42
	s_lshl_b32 s36, s30, 15
	s_add_u32 s54, s6, s36
	s_addc_u32 s55, s7, 0
	s_mov_b64 s[40:41], s[54:55]
	s_mov_b32 s45, 0
	s_mov_b32 s58, 0x40000
	s_mov_b32 s46, 0x180000
	s_mov_b64 s[48:49], s[12:13]
	s_cmp_lg_u64 s[14:15], 0
	s_cselect_b32 s57, 1, 0
	s_cmp_lg_u64 s[0:1], 0
	s_cselect_b32 s59, 1, 0
	s_mov_b32 s47, 0
	s_mov_b32 s60, 0
	s_mov_b32 s44, 0
	s_add_u32 s52, s50, 8
	s_addc_u32 s53, s51, 0
	global_load_dwordx2 v[174:175], v243, s[52:53] nt
	s_add_u32 s52, s50, 0x200000
	s_addc_u32 s53, s51, 0
	s_waitcnt vmcnt(1)
	v_cvt_f32_f16_e32 v250, v170
	v_cvt_f32_f16_sdwa v251, v170 dst_sel:DWORD dst_unused:UNUSED_PAD src0_sel:WORD_1
	v_cvt_f32_f16_e32 v252, v171
	v_cvt_f32_f16_sdwa v253, v171 dst_sel:DWORD dst_unused:UNUSED_PAD src0_sel:WORD_1
	v_pk_add_f32 v[198:199], v[130:131], v[134:135]
	v_pk_add_f32 v[200:201], v[132:133], v[136:137]
	v_mov_b32_e32 v194, 0
	v_mov_b32_e32 v195, 0
	v_mov_b32_e32 v196, 0
	v_mov_b32_e32 v197, 0
	v_pk_add_f32 v[198:199], v[198:199], v[250:251]
	v_pk_add_f32 v[200:201], v[200:201], v[252:253]
	s_branch .Lrec_act

.Lrec_own_mf:
	s_waitcnt lgkmcnt(3)
	v_mfma_f32_16x16x32_f16 v[158:161], v[2:5], v[138:141], v[130:133]
	v_mfma_f32_16x16x32_f16 v[154:157], v[66:69], v[138:141], v[134:137]
	s_waitcnt lgkmcnt(2)
	v_mfma_f32_16x16x32_f16 v[158:161], v[6:9], v[142:145], v[158:161]
	v_mfma_f32_16x16x32_f16 v[154:157], v[70:73], v[142:145], v[154:157]
	s_waitcnt lgkmcnt(1)
	v_mfma_f32_16x16x32_f16 v[158:161], v[10:13], v[146:149], v[158:161]
	v_mfma_f32_16x16x32_f16 v[154:157], v[74:77], v[146:149], v[154:157]
	s_waitcnt lgkmcnt(0)
	v_mfma_f32_16x16x32_f16 v[158:161], v[14:17], v[150:153], v[158:161]
	v_mfma_f32_16x16x32_f16 v[154:157], v[78:81], v[150:153], v[154:157]
	v_or3_b32 v249, v138, v139, v140
	v_or3_b32 v249, v249, v141, v142
	v_or3_b32 v249, v249, v143, v144
	v_or3_b32 v249, v249, v145, v146
	v_or3_b32 v249, v249, v147, v148
	v_or3_b32 v249, v249, v149, v150
	v_or3_b32 v249, v249, v151, v152
	v_bitop3_b32 v249, v249, s31, v153 bitop3:0xc8
	v_cmp_eq_u32_e32 vcc, 0, v249
	s_cmp_eq_u64 vcc, exec
	s_cbranch_scc0 .Lrec_own_retry
.Lrec_own_ok:
	s_barrier
	ds_read_b128 v[194:197], v180
	ds_read_b128 v[198:201], v181
	ds_read_b128 v[202:205], v182
	ds_read_b128 v[206:209], v183
	ds_read_b128 v[210:213], v184
	ds_read_b128 v[214:217], v185
	ds_read_b128 v[218:221], v186
	ds_read_b128 v[222:225], v187
	ds_read_b128 v[226:229], v188
	ds_read_b128 v[230:233], v189
	ds_read_b128 v[234:237], v190
	ds_read_b128 v[238:241], v191
	s_cmp_eq_u32 s59, 0
	s_cbranch_scc1 .Lrec_tail1
.Lrec_tail0:
	s_waitcnt lgkmcnt(11)
	v_mfma_f32_16x16x32_f16 v[154:157], v[82:85], v[194:197], v[154:157]
	s_waitcnt lgkmcnt(10)
	v_mfma_f32_16x16x32_f16 v[154:157], v[86:89], v[198:201], v[154:157]
	global_load_dwordx2 v[174:175], v243, s[52:53] nt
	s_waitcnt lgkmcnt(9)
	v_mfma_f32_16x16x32_f16 v[154:157], v[90:93], v[202:205], v[154:157]
	global_store_dword v242, v193, s[48:49] nt
	s_waitcnt lgkmcnt(8)
	v_mfma_f32_16x16x32_f16 v[154:157], v[94:97], v[206:209], v[154:157]
	s_mov_b64 exec, s[2:3]
	s_cmp_lg_u32 s57, 0
	s_cbranch_scc1 .Lrec_poi_sc1_0
	buffer_store_dwordx2 v[172:173], v165, s[8:11], s46 offen
	s_branch .Lrec_poi_done_0

.Lrec_poi_done_0:
	s_mov_b64 exec, -1
	s_waitcnt lgkmcnt(7)
	v_mfma_f32_16x16x32_f16 v[154:157], v[98:101], v[210:213], v[154:157]
	s_waitcnt lgkmcnt(6)
	v_mfma_f32_16x16x32_f16 v[154:157], v[102:105], v[214:217], v[154:157]
	s_xor_b32 s42, s42, 0x8000
	s_mov_b32 m0, s42
	s_and_b32 s36, s33, 7
	s_lshl_b32 s36, s36, 18
	s_add_u32 s40, s54, s36
	s_addc_u32 s41, s55, 0
	s_waitcnt lgkmcnt(5)
	v_mfma_f32_16x16x32_f16 v[154:157], v[106:109], v[218:221], v[154:157]
	s_add_i32 s58, s33, 1
	s_and_b32 s58, s58, 7
	s_lshl_b32 s58, s58, 18
	s_add_i32 s46, s33, 6
	s_and_b32 s46, s46, 7
	s_lshl_b32 s46, s46, 18
	s_waitcnt lgkmcnt(4)
	v_mfma_f32_16x16x32_f16 v[154:157], v[110:113], v[222:225], v[154:157]
	s_add_u32 s48, s48, 0x80000
	s_addc_u32 s49, s49, 0
	s_add_i32 s36, s33, 2
	s_min_u32 s36, s36, 0xff
	s_lshr_b32 s37, s36, 1
	s_lshl_b32 s37, s37, 21
	s_waitcnt lgkmcnt(3)
	v_mfma_f32_16x16x32_f16 v[154:157], v[114:117], v[226:229], v[154:157]
	s_and_b32 s36, s36, 1
	s_lshl_b32 s36, s36, 3
	s_or_b32 s37, s37, s36
	s_add_u32 s52, s50, s37
	s_addc_u32 s53, s51, 0
	s_waitcnt lgkmcnt(2)
	v_mfma_f32_16x16x32_f16 v[154:157], v[118:121], v[230:233], v[154:157]
	s_waitcnt lgkmcnt(1)
	v_mfma_f32_16x16x32_f16 v[154:157], v[122:125], v[234:237], v[154:157]
	s_waitcnt lgkmcnt(0)
	v_mfma_f32_16x16x32_f16 v[154:157], v[126:129], v[238:241], v[154:157]
	v_mfma_f32_16x16x32_f16 v[158:161], v[18:21], v[194:197], v[158:161]
	v_mfma_f32_16x16x32_f16 v[158:161], v[22:25], v[198:201], v[158:161]
	v_mfma_f32_16x16x32_f16 v[158:161], v[26:29], v[202:205], v[158:161]
	v_mfma_f32_16x16x32_f16 v[158:161], v[30:33], v[206:209], v[158:161]
	s_nop 3
	ds_write_b128 v178, v[154:157]
	v_mfma_f32_16x16x32_f16 v[158:161], v[34:37], v[210:213], v[158:161]
	v_mfma_f32_16x16x32_f16 v[158:161], v[38:41], v[214:217], v[158:161]
	v_mfma_f32_16x16x32_f16 v[158:161], v[42:45], v[218:221], v[158:161]
	v_mfma_f32_16x16x32_f16 v[158:161], v[46:49], v[222:225], v[158:161]
	s_waitcnt lgkmcnt(0)
	s_barrier
	ds_read_b128 v[194:197], v179
	v_mfma_f32_16x16x32_f16 v[158:161], v[50:53], v[226:229], v[158:161]
	v_mfma_f32_16x16x32_f16 v[158:161], v[54:57], v[230:233], v[158:161]
	v_mfma_f32_16x16x32_f16 v[158:161], v[58:61], v[234:237], v[158:161]
	v_mfma_f32_16x16x32_f16 v[158:161], v[62:65], v[238:241], v[158:161]
	s_nop 7
	v_pk_add_f32 v[198:199], v[158:159], v[250:251]
	v_pk_add_f32 v[200:201], v[160:161], v[252:253]
	s_branch .Lrec_act
.Lrec_tail1:
	s_waitcnt lgkmcnt(11)
	v_mfma_f32_16x16x32_f16 v[158:161], v[18:21], v[194:197], v[158:161]
	s_waitcnt lgkmcnt(10)
	v_mfma_f32_16x16x32_f16 v[158:161], v[22:25], v[198:201], v[158:161]
	global_load_dwordx2 v[174:175], v243, s[52:53] nt
	s_waitcnt lgkmcnt(9)
	v_mfma_f32_16x16x32_f16 v[158:161], v[26:29], v[202:205], v[158:161]
	global_store_dword v242, v193, s[48:49] nt
	s_waitcnt lgkmcnt(8)
	v_mfma_f32_16x16x32_f16 v[158:161], v[30:33], v[206:209], v[158:161]
	s_mov_b64 exec, s[2:3]
	s_cmp_lg_u32 s57, 0
	s_cbranch_scc1 .Lrec_poi_sc1_1
	buffer_store_dwordx2 v[172:173], v165, s[8:11], s46 offen
	s_branch .Lrec_poi_done_1

.Lrec_poi_done_1:
	s_mov_b64 exec, -1
	s_waitcnt lgkmcnt(7)
	v_mfma_f32_16x16x32_f16 v[158:161], v[34:37], v[210:213], v[158:161]
	s_waitcnt lgkmcnt(6)
	v_mfma_f32_16x16x32_f16 v[158:161], v[38:41], v[214:217], v[158:161]
	s_xor_b32 s42, s42, 0x8000
	s_mov_b32 m0, s42
	s_and_b32 s36, s33, 7
	s_lshl_b32 s36, s36, 18
	s_add_u32 s40, s54, s36
	s_addc_u32 s41, s55, 0
	s_waitcnt lgkmcnt(5)
	v_mfma_f32_16x16x32_f16 v[158:161], v[42:45], v[218:221], v[158:161]
	s_add_i32 s58, s33, 1
	s_and_b32 s58, s58, 7
	s_lshl_b32 s58, s58, 18
	s_add_i32 s46, s33, 6
	s_and_b32 s46, s46, 7
	s_lshl_b32 s46, s46, 18
	s_waitcnt lgkmcnt(4)
	v_mfma_f32_16x16x32_f16 v[158:161], v[46:49], v[222:225], v[158:161]
	s_add_u32 s48, s48, 0x80000
	s_addc_u32 s49, s49, 0
	s_add_i32 s36, s33, 2
	s_min_u32 s36, s36, 0xff
	s_lshr_b32 s37, s36, 1
	s_lshl_b32 s37, s37, 21
	s_waitcnt lgkmcnt(3)
	v_mfma_f32_16x16x32_f16 v[158:161], v[50:53], v[226:229], v[158:161]
	s_and_b32 s36, s36, 1
	s_lshl_b32 s36, s36, 3
	s_or_b32 s37, s37, s36
	s_add_u32 s52, s50, s37
	s_addc_u32 s53, s51, 0
	s_waitcnt lgkmcnt(2)
	v_mfma_f32_16x16x32_f16 v[158:161], v[54:57], v[230:233], v[158:161]
	s_waitcnt lgkmcnt(1)
	v_mfma_f32_16x16x32_f16 v[158:161], v[58:61], v[234:237], v[158:161]
	s_waitcnt lgkmcnt(0)
	v_mfma_f32_16x16x32_f16 v[158:161], v[62:65], v[238:241], v[158:161]
	v_mfma_f32_16x16x32_f16 v[154:157], v[82:85], v[194:197], v[154:157]
	v_mfma_f32_16x16x32_f16 v[154:157], v[86:89], v[198:201], v[154:157]
	v_mfma_f32_16x16x32_f16 v[154:157], v[90:93], v[202:205], v[154:157]
	v_mfma_f32_16x16x32_f16 v[154:157], v[94:97], v[206:209], v[154:157]
	s_nop 3
	ds_write_b128 v178, v[158:161]
	v_mfma_f32_16x16x32_f16 v[154:157], v[98:101], v[210:213], v[154:157]
	v_mfma_f32_16x16x32_f16 v[154:157], v[102:105], v[214:217], v[154:157]
	v_mfma_f32_16x16x32_f16 v[154:157], v[106:109], v[218:221], v[154:157]
	v_mfma_f32_16x16x32_f16 v[154:157], v[110:113], v[222:225], v[154:157]
	s_waitcnt lgkmcnt(0)
	s_barrier
	ds_read_b128 v[194:197], v179
	v_mfma_f32_16x16x32_f16 v[154:157], v[114:117], v[226:229], v[154:157]
	v_mfma_f32_16x16x32_f16 v[154:157], v[118:121], v[230:233], v[154:157]
	v_mfma_f32_16x16x32_f16 v[154:157], v[122:125], v[234:237], v[154:157]
	v_mfma_f32_16x16x32_f16 v[154:157], v[126:129], v[238:241], v[154:157]
	s_nop 7
	v_pk_add_f32 v[198:199], v[154:155], v[250:251]
	v_pk_add_f32 v[200:201], v[156:157], v[252:253]

.Lrec_own_retry:
	s_cmp_lg_u32 s47, 0
	s_cbranch_scc1 .Lrec_own_ok
	s_add_i32 s44, s44, 1
	s_cmp_gt_u32 s44, 0x2000
	s_cbranch_scc1 .Lrec_own_die
	global_load_lds_dwordx4 v176, s[40:41] sc1
	global_load_lds_dwordx4 v176, s[40:41] offset:1024 sc1
	global_load_lds_dwordx4 v176, s[40:41] offset:2048 sc1
	global_load_lds_dwordx4 v176, s[40:41] offset:3072 sc1
	s_waitcnt vmcnt(0)
	ds_read_b128 v[138:141], v166
	ds_read_b128 v[142:145], v166 offset:1024
	ds_read_b128 v[146:149], v166 offset:2048
	ds_read_b128 v[150:153], v166 offset:3072
	s_branch .Lrec_own_mf

amdhsa.kernels:
  - .agpr_count:     0
    .args:
      - .actual_access:  read_only
        .address_space:  global
        .offset:         0
        .size:           8
        .value_kind:     global_buffer
      - .actual_access:  write_only
        .address_space:  global
        .offset:         8
        .size:           8
        .value_kind:     global_buffer
      - .actual_access:  read_only
        .address_space:  global
        .offset:         16
        .size:           8
        .value_kind:     global_buffer
      - .actual_access:  read_only
        .address_space:  global
        .offset:         24
        .size:           8
        .value_kind:     global_buffer
      - .actual_access:  read_only
        .address_space:  global
        .offset:         32
        .size:           8
        .value_kind:     global_buffer
      - .actual_access:  read_only
        .address_space:  global
        .offset:         40
        .size:           8
        .value_kind:     global_buffer
      - .actual_access:  read_only
        .address_space:  global
        .offset:         48
        .size:           8
        .value_kind:     global_buffer
      - .actual_access:  read_only
        .address_space:  global
        .offset:         56
        .size:           8
        .value_kind:     global_buffer
      - .actual_access:  read_only
        .address_space:  global
        .offset:         64
        .size:           8
        .value_kind:     global_buffer
      - .actual_access:  read_only
        .address_space:  global
        .offset:         72
        .size:           8
        .value_kind:     global_buffer
      - .actual_access:  write_only
        .address_space:  global
        .offset:         80
        .size:           8
        .value_kind:     global_buffer
      - .actual_access:  write_only
        .address_space:  global
        .offset:         88
        .size:           8
        .value_kind:     global_buffer
      - .actual_access:  write_only
        .address_space:  global
        .offset:         96
        .size:           8
        .value_kind:     global_buffer
      - .actual_access:  write_only
        .address_space:  global
        .offset:         104
        .size:           8
        .value_kind:     global_buffer
    .group_segment_fixed_size: 0
    .kernarg_segment_align: 8
    .kernarg_segment_size: 112
    .language:       OpenCL C
    .language_version:
      - 2
      - 0
    .max_flat_workgroup_size: 256
    .name:           _Z4prepPKfPDF16_S0_S0_S0_S0_S0_S0_S0_S0_S1_S1_PfPh
    .private_segment_fixed_size: 0
    .sgpr_count:     32
    .sgpr_spill_count: 0
    .symbol:         _Z4prepPKfPDF16_S0_S0_S0_S0_S0_S0_S0_S0_S1_S1_PfPh.kd
    .uniform_work_group_size: 1
    .uses_dynamic_stack: false
    .vgpr_count:     16
    .vgpr_spill_count: 0
    .wavefront_size: 64
  - .agpr_count:     0
    .args:
      - .address_space:  global
        .offset:         0
        .size:           8
        .value_kind:     global_buffer
      - .address_space:  global
        .offset:         8
        .size:           8
        .value_kind:     global_buffer
      - .actual_access:  write_only
        .address_space:  global
        .offset:         16
        .size:           8
        .value_kind:     global_buffer
    .group_segment_fixed_size: 0
    .kernarg_segment_align: 8
    .kernarg_segment_size: 24
    .language:       OpenCL C
    .language_version:
      - 2
      - 0
    .max_flat_workgroup_size: 512
    .name:           _Z7gemm_zxPKDF16_S0_PDF16_
    .private_segment_fixed_size: 0
    .sgpr_count:     48
    .sgpr_spill_count: 0
    .symbol:         _Z7gemm_zxPKDF16_S0_PDF16_.kd
    .uniform_work_group_size: 1
    .uses_dynamic_stack: false
    .vgpr_count:     256
    .vgpr_spill_count: 0
    .wavefront_size: 64
  - .agpr_count:     0
    .args:
      - .actual_access:  read_only
        .address_space:  global
        .offset:         0
        .size:           8
        .value_kind:     global_buffer
      - .actual_access:  read_only
        .address_space:  global
        .offset:         8
        .size:           8
        .value_kind:     global_buffer
      - .actual_access:  read_only
        .address_space:  global
        .offset:         16
        .size:           8
        .value_kind:     global_buffer
      - .address_space:  global
        .offset:         24
        .size:           8
        .value_kind:     global_buffer
      - .actual_access:  write_only
        .address_space:  global
        .offset:         32
        .size:           8
        .value_kind:     global_buffer
    .group_segment_fixed_size: 73728
    .kernarg_segment_align: 8
    .kernarg_segment_size: 40
    .language:       OpenCL C
    .language_version:
      - 2
      - 0
    .max_flat_workgroup_size: 512
    .name:           _Z8lstm_recPKDF16_S0_PKfPhPf
    .private_segment_fixed_size: 0
    .sgpr_count:     80
    .sgpr_spill_count: 0
    .symbol:         _Z8lstm_recPKDF16_S0_PKfPhPf.kd
    .uniform_work_group_size: 1
    .uses_dynamic_stack: false
    .vgpr_count:     256
    .vgpr_spill_count: 0
    .wavefront_size: 64
